# grid barriers 2..13: early L1 invalidate issued just BEFORE the arrival atomic (previous version: just after)
# baseline (speedup 1.0000x reference)
; __device__ __forceinline__ unsigned xb_ld(unsigned* p)              { return __hip_atomic_load(p, __ATOMIC_RELAXED, __HIP_MEMORY_SCOPE_AGENT); }
; __device__ __forceinline__ unsigned xb_add(unsigned* p, unsigned v) { return __hip_atomic_fetch_add(p, v, __ATOMIC_RELAXED, __HIP_MEMORY_SCOPE_AGENT); }
; #define XB_SPIN(cond, bar) do { unsigned _sp = 0; while (cond) { __builtin_amdgcn_s_sleep(1); \
;     if ((++_sp & 255u) == 0u) { if (xb_ld(&(bar)[XB_TMO])) break; if (_sp > XB_SPIN_CAP) { atomicAdd(&(bar)[XB_TMO], 1u); break; } } } } while (0)
; __device__ __forceinline__ void xcd_barrier(const XcdBarrier& b) {
;   asm volatile("s_waitcnt vmcnt(0)" ::: "memory");
;   __syncthreads();
;   if (threadIdx.x == 0) {
;     unsigned* bar = b.bar;
;     __builtin_amdgcn_s_waitcnt(0);
;     unsigned nloc = b.st[0], nx = b.st[1];
;     if (nloc == 0u) { xcd_barrier_complete(bar, b.x, nloc, nx); b.st[0] = nloc; b.st[1] = nx; }
;     const unsigned old = xb_add(&bar[XB_XSUB(b.x)], 1u);
;     const unsigned gen = old / nloc;
;     if (old + 1u == (gen + 1u) * nloc) {
;       __builtin_amdgcn_fence(__ATOMIC_RELEASE, "agent");
;       asm volatile("s_waitcnt vmcnt(0)" ::: "memory");
;       const unsigned og = xb_add(&bar[XB_TOP], 1u);
;       const unsigned tg = og / nx;
;       if (og + 1u == (tg + 1u) * nx) xb_add(&bar[XB_TOPGEN], 1u);
;       else XB_SPIN(xb_ld(&bar[XB_TOPGEN]) == tg, bar);
;       __builtin_amdgcn_fence(__ATOMIC_ACQUIRE, "agent");
;       xb_add(&bar[XB_XGEN(b.x)], 1u);
;       asm volatile("s_waitcnt vmcnt(0)" ::: "memory");
;     } else {
;       XB_SPIN(xb_ld(&bar[XB_XGEN(b.x)]) == gen, bar);
;       __builtin_amdgcn_fence(__ATOMIC_ACQUIRE, "agent");
;       asm volatile("s_waitcnt vmcnt(0)" ::: "memory");
;     }
;   }
;   __syncthreads();
; }
.LBB0_115:
	s_waitcnt vmcnt(0)
	s_barrier
	s_and_saveexec_b64 s[6:7], s[4:5]
	s_cbranch_execz .LBB0_167
	s_waitcnt vmcnt(0) lgkmcnt(0)
	s_add_u32 s98, s98, 1
	v_mov_b32_e32 v253, 0x12810
	ds_read_b32 v254, v253
	ds_read_b32 v253, v253 offset:4
	s_lshl_b32 s101, s33, 8
	s_add_u32 s99, s101, 5120
	s_waitcnt lgkmcnt(0)
	v_readfirstlane_b32 s100, v254
	v_mov_b32_e32 v254, s99
	v_readfirstlane_b32 s99, v253
	s_nop 0
	v_mov_b32_e32 v253, v254
	v_mov_b32_e32 v254, 1
	buffer_inv sc1
	global_atomic_add v254, v253, v254, s[44:45] offset:64 sc0
	s_mul_i32 s100, s100, s98
	s_mul_i32 s99, s99, s98
	s_waitcnt vmcnt(0)
	v_add_u32_e32 v254, 1, v254
	v_cmp_ne_u32_e32 vcc, s100, v254
	s_cbranch_vccnz .Lgb_wait_2
	buffer_wbl2 sc1
	s_waitcnt vmcnt(0)
	v_mov_b32_e32 v254, 1
	v_mov_b32_e32 v253, 9216
	global_atomic_add v253, v254, s[44:45] offset:64
	global_atomic_add v253, v254, s[44:45] offset:320
	global_atomic_add v253, v254, s[44:45] offset:576
	global_atomic_add v253, v254, s[44:45] offset:832
	global_atomic_add v253, v254, s[44:45] offset:1088
	global_atomic_add v253, v254, s[44:45] offset:1344
	global_atomic_add v253, v254, s[44:45] offset:1600
	global_atomic_add v253, v254, s[44:45] offset:1856
	v_mov_b32_e32 v253, 11264
	global_atomic_add v253, v254, s[44:45] offset:64
	global_atomic_add v253, v254, s[44:45] offset:320
	global_atomic_add v253, v254, s[44:45] offset:576
	global_atomic_add v253, v254, s[44:45] offset:832
	global_atomic_add v253, v254, s[44:45] offset:1088
	global_atomic_add v253, v254, s[44:45] offset:1344
	global_atomic_add v253, v254, s[44:45] offset:1600
	global_atomic_add v253, v254, s[44:45] offset:1856

; __device__ __forceinline__ unsigned xb_ld(unsigned* p)              { return __hip_atomic_load(p, __ATOMIC_RELAXED, __HIP_MEMORY_SCOPE_AGENT); }
; __device__ __forceinline__ unsigned xb_add(unsigned* p, unsigned v) { return __hip_atomic_fetch_add(p, v, __ATOMIC_RELAXED, __HIP_MEMORY_SCOPE_AGENT); }
; #define XB_SPIN(cond, bar) do { unsigned _sp = 0; while (cond) { __builtin_amdgcn_s_sleep(1); \
;     if ((++_sp & 255u) == 0u) { if (xb_ld(&(bar)[XB_TMO])) break; if (_sp > XB_SPIN_CAP) { atomicAdd(&(bar)[XB_TMO], 1u); break; } } } } while (0)
; __device__ __forceinline__ void xcd_barrier(const XcdBarrier& b) {
;   asm volatile("s_waitcnt vmcnt(0)" ::: "memory");
;   __syncthreads();
;   if (threadIdx.x == 0) {
;     unsigned* bar = b.bar;
;     __builtin_amdgcn_s_waitcnt(0);
;     unsigned nloc = b.st[0], nx = b.st[1];
;     if (nloc == 0u) { xcd_barrier_complete(bar, b.x, nloc, nx); b.st[0] = nloc; b.st[1] = nx; }
;     const unsigned old = xb_add(&bar[XB_XSUB(b.x)], 1u);
;     const unsigned gen = old / nloc;
;     if (old + 1u == (gen + 1u) * nloc) {
;       __builtin_amdgcn_fence(__ATOMIC_RELEASE, "agent");
;       asm volatile("s_waitcnt vmcnt(0)" ::: "memory");
;       const unsigned og = xb_add(&bar[XB_TOP], 1u);
;       const unsigned tg = og / nx;
;       if (og + 1u == (tg + 1u) * nx) xb_add(&bar[XB_TOPGEN], 1u);
;       else XB_SPIN(xb_ld(&bar[XB_TOPGEN]) == tg, bar);
;       __builtin_amdgcn_fence(__ATOMIC_ACQUIRE, "agent");
;       xb_add(&bar[XB_XGEN(b.x)], 1u);
;       asm volatile("s_waitcnt vmcnt(0)" ::: "memory");
;     } else {
;       XB_SPIN(xb_ld(&bar[XB_XGEN(b.x)]) == gen, bar);
;       __builtin_amdgcn_fence(__ATOMIC_ACQUIRE, "agent");
;       asm volatile("s_waitcnt vmcnt(0)" ::: "memory");
;     }
;   }
;   __syncthreads();
; }
.LBB0_179:
	s_or_b64 exec, exec, s[10:11]
	s_waitcnt vmcnt(0)
	s_barrier
	s_and_saveexec_b64 s[6:7], s[4:5]
	s_cbranch_execz .LBB0_231
	s_waitcnt vmcnt(0) lgkmcnt(0)
	s_add_u32 s98, s98, 1
	v_mov_b32_e32 v253, 0x12810
	ds_read_b32 v254, v253
	ds_read_b32 v253, v253 offset:4
	s_lshl_b32 s101, s33, 8
	s_add_u32 s99, s101, 5120
	s_waitcnt lgkmcnt(0)
	v_readfirstlane_b32 s100, v254
	v_mov_b32_e32 v254, s99
	v_readfirstlane_b32 s99, v253
	s_nop 0
	v_mov_b32_e32 v253, v254
	v_mov_b32_e32 v254, 1
	buffer_inv sc1
	global_atomic_add v254, v253, v254, s[44:45] offset:64 sc0
	s_mul_i32 s100, s100, s98
	s_mul_i32 s99, s99, s98
	s_waitcnt vmcnt(0)
	v_add_u32_e32 v254, 1, v254
	v_cmp_ne_u32_e32 vcc, s100, v254
	s_cbranch_vccnz .Lgb_wait_3
	buffer_wbl2 sc1
	s_waitcnt vmcnt(0)
	v_mov_b32_e32 v254, 1
	v_mov_b32_e32 v253, 9216
	global_atomic_add v253, v254, s[44:45] offset:64
	global_atomic_add v253, v254, s[44:45] offset:320
	global_atomic_add v253, v254, s[44:45] offset:576
	global_atomic_add v253, v254, s[44:45] offset:832
	global_atomic_add v253, v254, s[44:45] offset:1088
	global_atomic_add v253, v254, s[44:45] offset:1344
	global_atomic_add v253, v254, s[44:45] offset:1600
	global_atomic_add v253, v254, s[44:45] offset:1856
	v_mov_b32_e32 v253, 11264
	global_atomic_add v253, v254, s[44:45] offset:64
	global_atomic_add v253, v254, s[44:45] offset:320
	global_atomic_add v253, v254, s[44:45] offset:576
	global_atomic_add v253, v254, s[44:45] offset:832
	global_atomic_add v253, v254, s[44:45] offset:1088
	global_atomic_add v253, v254, s[44:45] offset:1344
	global_atomic_add v253, v254, s[44:45] offset:1600
	global_atomic_add v253, v254, s[44:45] offset:1856

; __device__ __forceinline__ unsigned xb_ld(unsigned* p)              { return __hip_atomic_load(p, __ATOMIC_RELAXED, __HIP_MEMORY_SCOPE_AGENT); }
; __device__ __forceinline__ unsigned xb_add(unsigned* p, unsigned v) { return __hip_atomic_fetch_add(p, v, __ATOMIC_RELAXED, __HIP_MEMORY_SCOPE_AGENT); }
; #define XB_SPIN(cond, bar) do { unsigned _sp = 0; while (cond) { __builtin_amdgcn_s_sleep(1); \
;     if ((++_sp & 255u) == 0u) { if (xb_ld(&(bar)[XB_TMO])) break; if (_sp > XB_SPIN_CAP) { atomicAdd(&(bar)[XB_TMO], 1u); break; } } } } while (0)
; __device__ __forceinline__ void xcd_barrier(const XcdBarrier& b) {
;   asm volatile("s_waitcnt vmcnt(0)" ::: "memory");
;   __syncthreads();
;   if (threadIdx.x == 0) {
;     unsigned* bar = b.bar;
;     __builtin_amdgcn_s_waitcnt(0);
;     unsigned nloc = b.st[0], nx = b.st[1];
;     if (nloc == 0u) { xcd_barrier_complete(bar, b.x, nloc, nx); b.st[0] = nloc; b.st[1] = nx; }
;     const unsigned old = xb_add(&bar[XB_XSUB(b.x)], 1u);
;     const unsigned gen = old / nloc;
;     if (old + 1u == (gen + 1u) * nloc) {
;       __builtin_amdgcn_fence(__ATOMIC_RELEASE, "agent");
;       asm volatile("s_waitcnt vmcnt(0)" ::: "memory");
;       const unsigned og = xb_add(&bar[XB_TOP], 1u);
;       const unsigned tg = og / nx;
;       if (og + 1u == (tg + 1u) * nx) xb_add(&bar[XB_TOPGEN], 1u);
;       else XB_SPIN(xb_ld(&bar[XB_TOPGEN]) == tg, bar);
;       __builtin_amdgcn_fence(__ATOMIC_ACQUIRE, "agent");
;       xb_add(&bar[XB_XGEN(b.x)], 1u);
;       asm volatile("s_waitcnt vmcnt(0)" ::: "memory");
;     } else {
;       XB_SPIN(xb_ld(&bar[XB_XGEN(b.x)]) == gen, bar);
;       __builtin_amdgcn_fence(__ATOMIC_ACQUIRE, "agent");
;       asm volatile("s_waitcnt vmcnt(0)" ::: "memory");
;     }
;   }
;   __syncthreads();
; }
.LBB0_572:
	s_waitcnt vmcnt(0)
	s_waitcnt lgkmcnt(0)
	s_barrier
	s_and_saveexec_b64 s[6:7], s[4:5]
	s_cbranch_execz .LBB0_624
	s_waitcnt vmcnt(0) lgkmcnt(0)
	s_add_u32 s98, s98, 1
	v_mov_b32_e32 v253, 0x12810
	ds_read_b32 v254, v253
	ds_read_b32 v253, v253 offset:4
	s_lshl_b32 s101, s33, 8
	s_add_u32 s99, s101, 5120
	s_waitcnt lgkmcnt(0)
	v_readfirstlane_b32 s100, v254
	v_mov_b32_e32 v254, s99
	v_readfirstlane_b32 s99, v253
	s_nop 0
	v_mov_b32_e32 v253, v254
	v_mov_b32_e32 v254, 1
	buffer_inv sc1
	global_atomic_add v254, v253, v254, s[44:45] offset:64 sc0
	s_mul_i32 s100, s100, s98
	s_mul_i32 s99, s99, s98
	s_waitcnt vmcnt(0)
	v_add_u32_e32 v254, 1, v254
	v_cmp_ne_u32_e32 vcc, s100, v254
	s_cbranch_vccnz .Lgb_wait_4
	buffer_wbl2 sc1
	s_waitcnt vmcnt(0)
	v_mov_b32_e32 v254, 1
	v_mov_b32_e32 v253, 9216
	global_atomic_add v253, v254, s[44:45] offset:64
	global_atomic_add v253, v254, s[44:45] offset:320
	global_atomic_add v253, v254, s[44:45] offset:576
	global_atomic_add v253, v254, s[44:45] offset:832
	global_atomic_add v253, v254, s[44:45] offset:1088
	global_atomic_add v253, v254, s[44:45] offset:1344
	global_atomic_add v253, v254, s[44:45] offset:1600
	global_atomic_add v253, v254, s[44:45] offset:1856
	v_mov_b32_e32 v253, 11264
	global_atomic_add v253, v254, s[44:45] offset:64
	global_atomic_add v253, v254, s[44:45] offset:320
	global_atomic_add v253, v254, s[44:45] offset:576
	global_atomic_add v253, v254, s[44:45] offset:832
	global_atomic_add v253, v254, s[44:45] offset:1088
	global_atomic_add v253, v254, s[44:45] offset:1344
	global_atomic_add v253, v254, s[44:45] offset:1600
	global_atomic_add v253, v254, s[44:45] offset:1856

; __device__ __forceinline__ unsigned xb_ld(unsigned* p)              { return __hip_atomic_load(p, __ATOMIC_RELAXED, __HIP_MEMORY_SCOPE_AGENT); }
; __device__ __forceinline__ unsigned xb_add(unsigned* p, unsigned v) { return __hip_atomic_fetch_add(p, v, __ATOMIC_RELAXED, __HIP_MEMORY_SCOPE_AGENT); }
; #define XB_SPIN(cond, bar) do { unsigned _sp = 0; while (cond) { __builtin_amdgcn_s_sleep(1); \
;     if ((++_sp & 255u) == 0u) { if (xb_ld(&(bar)[XB_TMO])) break; if (_sp > XB_SPIN_CAP) { atomicAdd(&(bar)[XB_TMO], 1u); break; } } } } while (0)
; __device__ __forceinline__ void xcd_barrier(const XcdBarrier& b) {
;   asm volatile("s_waitcnt vmcnt(0)" ::: "memory");
;   __syncthreads();
;   if (threadIdx.x == 0) {
;     unsigned* bar = b.bar;
;     __builtin_amdgcn_s_waitcnt(0);
;     unsigned nloc = b.st[0], nx = b.st[1];
;     if (nloc == 0u) { xcd_barrier_complete(bar, b.x, nloc, nx); b.st[0] = nloc; b.st[1] = nx; }
;     const unsigned old = xb_add(&bar[XB_XSUB(b.x)], 1u);
;     const unsigned gen = old / nloc;
;     if (old + 1u == (gen + 1u) * nloc) {
;       __builtin_amdgcn_fence(__ATOMIC_RELEASE, "agent");
;       asm volatile("s_waitcnt vmcnt(0)" ::: "memory");
;       const unsigned og = xb_add(&bar[XB_TOP], 1u);
;       const unsigned tg = og / nx;
;       if (og + 1u == (tg + 1u) * nx) xb_add(&bar[XB_TOPGEN], 1u);
;       else XB_SPIN(xb_ld(&bar[XB_TOPGEN]) == tg, bar);
;       __builtin_amdgcn_fence(__ATOMIC_ACQUIRE, "agent");
;       xb_add(&bar[XB_XGEN(b.x)], 1u);
;       asm volatile("s_waitcnt vmcnt(0)" ::: "memory");
;     } else {
;       XB_SPIN(xb_ld(&bar[XB_XGEN(b.x)]) == gen, bar);
;       __builtin_amdgcn_fence(__ATOMIC_ACQUIRE, "agent");
;       asm volatile("s_waitcnt vmcnt(0)" ::: "memory");
;     }
;   }
;   __syncthreads();
; }
.LBB0_677:
	s_or_b64 exec, exec, s[12:13]
	s_waitcnt vmcnt(0)
	s_waitcnt lgkmcnt(0)
	s_barrier
	s_and_saveexec_b64 s[6:7], s[4:5]
	s_cbranch_execz .LBB0_729
	s_waitcnt vmcnt(0) lgkmcnt(0)
	s_add_u32 s98, s98, 1
	v_mov_b32_e32 v253, 0x12810
	ds_read_b32 v254, v253
	ds_read_b32 v253, v253 offset:4
	s_lshl_b32 s101, s33, 8
	s_add_u32 s99, s101, 5120
	s_waitcnt lgkmcnt(0)
	v_readfirstlane_b32 s100, v254
	v_mov_b32_e32 v254, s99
	v_readfirstlane_b32 s99, v253
	s_nop 0
	v_mov_b32_e32 v253, v254
	v_mov_b32_e32 v254, 1
	buffer_inv sc1
	global_atomic_add v254, v253, v254, s[44:45] offset:64 sc0
	s_mul_i32 s100, s100, s98
	s_mul_i32 s99, s99, s98
	s_waitcnt vmcnt(0)
	v_add_u32_e32 v254, 1, v254
	v_cmp_ne_u32_e32 vcc, s100, v254
	s_cbranch_vccnz .Lgb_wait_5
	buffer_wbl2 sc1
	s_waitcnt vmcnt(0)
	v_mov_b32_e32 v254, 1
	v_mov_b32_e32 v253, 9216
	global_atomic_add v253, v254, s[44:45] offset:64
	global_atomic_add v253, v254, s[44:45] offset:320
	global_atomic_add v253, v254, s[44:45] offset:576
	global_atomic_add v253, v254, s[44:45] offset:832
	global_atomic_add v253, v254, s[44:45] offset:1088
	global_atomic_add v253, v254, s[44:45] offset:1344
	global_atomic_add v253, v254, s[44:45] offset:1600
	global_atomic_add v253, v254, s[44:45] offset:1856
	v_mov_b32_e32 v253, 11264
	global_atomic_add v253, v254, s[44:45] offset:64
	global_atomic_add v253, v254, s[44:45] offset:320
	global_atomic_add v253, v254, s[44:45] offset:576
	global_atomic_add v253, v254, s[44:45] offset:832
	global_atomic_add v253, v254, s[44:45] offset:1088
	global_atomic_add v253, v254, s[44:45] offset:1344
	global_atomic_add v253, v254, s[44:45] offset:1600
	global_atomic_add v253, v254, s[44:45] offset:1856

; __device__ __forceinline__ unsigned xb_ld(unsigned* p)              { return __hip_atomic_load(p, __ATOMIC_RELAXED, __HIP_MEMORY_SCOPE_AGENT); }
; __device__ __forceinline__ unsigned xb_add(unsigned* p, unsigned v) { return __hip_atomic_fetch_add(p, v, __ATOMIC_RELAXED, __HIP_MEMORY_SCOPE_AGENT); }
; #define XB_SPIN(cond, bar) do { unsigned _sp = 0; while (cond) { __builtin_amdgcn_s_sleep(1); \
;     if ((++_sp & 255u) == 0u) { if (xb_ld(&(bar)[XB_TMO])) break; if (_sp > XB_SPIN_CAP) { atomicAdd(&(bar)[XB_TMO], 1u); break; } } } } while (0)
; __device__ __forceinline__ void xcd_barrier(const XcdBarrier& b) {
;   asm volatile("s_waitcnt vmcnt(0)" ::: "memory");
;   __syncthreads();
;   if (threadIdx.x == 0) {
;     unsigned* bar = b.bar;
;     __builtin_amdgcn_s_waitcnt(0);
;     unsigned nloc = b.st[0], nx = b.st[1];
;     if (nloc == 0u) { xcd_barrier_complete(bar, b.x, nloc, nx); b.st[0] = nloc; b.st[1] = nx; }
;     const unsigned old = xb_add(&bar[XB_XSUB(b.x)], 1u);
;     const unsigned gen = old / nloc;
;     if (old + 1u == (gen + 1u) * nloc) {
;       __builtin_amdgcn_fence(__ATOMIC_RELEASE, "agent");
;       asm volatile("s_waitcnt vmcnt(0)" ::: "memory");
;       const unsigned og = xb_add(&bar[XB_TOP], 1u);
;       const unsigned tg = og / nx;
;       if (og + 1u == (tg + 1u) * nx) xb_add(&bar[XB_TOPGEN], 1u);
;       else XB_SPIN(xb_ld(&bar[XB_TOPGEN]) == tg, bar);
;       __builtin_amdgcn_fence(__ATOMIC_ACQUIRE, "agent");
;       xb_add(&bar[XB_XGEN(b.x)], 1u);
;       asm volatile("s_waitcnt vmcnt(0)" ::: "memory");
;     } else {
;       XB_SPIN(xb_ld(&bar[XB_XGEN(b.x)]) == gen, bar);
;       __builtin_amdgcn_fence(__ATOMIC_ACQUIRE, "agent");
;       asm volatile("s_waitcnt vmcnt(0)" ::: "memory");
;     }
;   }
;   __syncthreads();
; }
.LBB0_1015:
	s_or_b64 exec, exec, s[12:13]
	s_waitcnt vmcnt(0)
	s_barrier
	s_and_saveexec_b64 s[12:13], s[4:5]
	s_cbranch_execz .LBB0_1067
	s_waitcnt vmcnt(0) lgkmcnt(0)
	s_add_u32 s98, s98, 1
	v_mov_b32_e32 v253, 0x12810
	ds_read_b32 v254, v253
	ds_read_b32 v253, v253 offset:4
	s_lshl_b32 s101, s33, 8
	s_add_u32 s99, s101, 5120
	s_waitcnt lgkmcnt(0)
	v_readfirstlane_b32 s100, v254
	v_mov_b32_e32 v254, s99
	v_readfirstlane_b32 s99, v253
	s_nop 0
	v_mov_b32_e32 v253, v254
	v_mov_b32_e32 v254, 1
	buffer_inv sc1
	global_atomic_add v254, v253, v254, s[44:45] offset:64 sc0
	s_mul_i32 s100, s100, s98
	s_mul_i32 s99, s99, s98
	s_waitcnt vmcnt(0)
	v_add_u32_e32 v254, 1, v254
	v_cmp_ne_u32_e32 vcc, s100, v254
	s_cbranch_vccnz .Lgb_wait_7
	buffer_wbl2 sc1
	s_waitcnt vmcnt(0)
	v_mov_b32_e32 v254, 1
	v_mov_b32_e32 v253, 9216
	global_atomic_add v253, v254, s[44:45] offset:64
	global_atomic_add v253, v254, s[44:45] offset:320
	global_atomic_add v253, v254, s[44:45] offset:576
	global_atomic_add v253, v254, s[44:45] offset:832
	global_atomic_add v253, v254, s[44:45] offset:1088
	global_atomic_add v253, v254, s[44:45] offset:1344
	global_atomic_add v253, v254, s[44:45] offset:1600
	global_atomic_add v253, v254, s[44:45] offset:1856
	v_mov_b32_e32 v253, 11264
	global_atomic_add v253, v254, s[44:45] offset:64
	global_atomic_add v253, v254, s[44:45] offset:320
	global_atomic_add v253, v254, s[44:45] offset:576
	global_atomic_add v253, v254, s[44:45] offset:832
	global_atomic_add v253, v254, s[44:45] offset:1088
	global_atomic_add v253, v254, s[44:45] offset:1344
	global_atomic_add v253, v254, s[44:45] offset:1600
	global_atomic_add v253, v254, s[44:45] offset:1856

; __device__ __forceinline__ unsigned xb_ld(unsigned* p)              { return __hip_atomic_load(p, __ATOMIC_RELAXED, __HIP_MEMORY_SCOPE_AGENT); }
; __device__ __forceinline__ unsigned xb_add(unsigned* p, unsigned v) { return __hip_atomic_fetch_add(p, v, __ATOMIC_RELAXED, __HIP_MEMORY_SCOPE_AGENT); }
; #define XB_SPIN(cond, bar) do { unsigned _sp = 0; while (cond) { __builtin_amdgcn_s_sleep(1); \
;     if ((++_sp & 255u) == 0u) { if (xb_ld(&(bar)[XB_TMO])) break; if (_sp > XB_SPIN_CAP) { atomicAdd(&(bar)[XB_TMO], 1u); break; } } } } while (0)
; __device__ __forceinline__ void xcd_barrier(const XcdBarrier& b) {
;   asm volatile("s_waitcnt vmcnt(0)" ::: "memory");
;   __syncthreads();
;   if (threadIdx.x == 0) {
;     unsigned* bar = b.bar;
;     __builtin_amdgcn_s_waitcnt(0);
;     unsigned nloc = b.st[0], nx = b.st[1];
;     if (nloc == 0u) { xcd_barrier_complete(bar, b.x, nloc, nx); b.st[0] = nloc; b.st[1] = nx; }
;     const unsigned old = xb_add(&bar[XB_XSUB(b.x)], 1u);
;     const unsigned gen = old / nloc;
;     if (old + 1u == (gen + 1u) * nloc) {
;       __builtin_amdgcn_fence(__ATOMIC_RELEASE, "agent");
;       asm volatile("s_waitcnt vmcnt(0)" ::: "memory");
;       const unsigned og = xb_add(&bar[XB_TOP], 1u);
;       const unsigned tg = og / nx;
;       if (og + 1u == (tg + 1u) * nx) xb_add(&bar[XB_TOPGEN], 1u);
;       else XB_SPIN(xb_ld(&bar[XB_TOPGEN]) == tg, bar);
;       __builtin_amdgcn_fence(__ATOMIC_ACQUIRE, "agent");
;       xb_add(&bar[XB_XGEN(b.x)], 1u);
;       asm volatile("s_waitcnt vmcnt(0)" ::: "memory");
;     } else {
;       XB_SPIN(xb_ld(&bar[XB_XGEN(b.x)]) == gen, bar);
;       __builtin_amdgcn_fence(__ATOMIC_ACQUIRE, "agent");
;       asm volatile("s_waitcnt vmcnt(0)" ::: "memory");
;     }
;   }
;   __syncthreads();
; }
.LBB0_1072:
	s_waitcnt vmcnt(0)
	s_waitcnt vmcnt(63) expcnt(7) lgkmcnt(15)
	s_barrier
	s_and_saveexec_b64 s[12:13], s[4:5]
	s_cbranch_execz .LBB0_1124
	s_waitcnt vmcnt(0) lgkmcnt(0)
	s_add_u32 s98, s98, 1
	v_mov_b32_e32 v253, 0x12810
	ds_read_b32 v254, v253
	ds_read_b32 v253, v253 offset:4
	s_lshl_b32 s101, s33, 8
	s_add_u32 s99, s101, 5120
	s_waitcnt lgkmcnt(0)
	v_readfirstlane_b32 s100, v254
	v_mov_b32_e32 v254, s99
	v_readfirstlane_b32 s99, v253
	s_nop 0
	v_mov_b32_e32 v253, v254
	v_mov_b32_e32 v254, 1
	buffer_inv sc1
	global_atomic_add v254, v253, v254, s[44:45] offset:64 sc0
	s_mul_i32 s100, s100, s98
	s_mul_i32 s99, s99, s98
	s_waitcnt vmcnt(0)
	v_add_u32_e32 v254, 1, v254
	v_cmp_ne_u32_e32 vcc, s100, v254
	s_cbranch_vccnz .Lgb_wait_8
	buffer_wbl2 sc1
	s_waitcnt vmcnt(0)
	v_mov_b32_e32 v254, 1
	v_mov_b32_e32 v253, 9216
	global_atomic_add v253, v254, s[44:45] offset:64
	global_atomic_add v253, v254, s[44:45] offset:320
	global_atomic_add v253, v254, s[44:45] offset:576
	global_atomic_add v253, v254, s[44:45] offset:832
	global_atomic_add v253, v254, s[44:45] offset:1088
	global_atomic_add v253, v254, s[44:45] offset:1344
	global_atomic_add v253, v254, s[44:45] offset:1600
	global_atomic_add v253, v254, s[44:45] offset:1856
	v_mov_b32_e32 v253, 11264
	global_atomic_add v253, v254, s[44:45] offset:64
	global_atomic_add v253, v254, s[44:45] offset:320
	global_atomic_add v253, v254, s[44:45] offset:576
	global_atomic_add v253, v254, s[44:45] offset:832
	global_atomic_add v253, v254, s[44:45] offset:1088
	global_atomic_add v253, v254, s[44:45] offset:1344
	global_atomic_add v253, v254, s[44:45] offset:1600
	global_atomic_add v253, v254, s[44:45] offset:1856

; __device__ __forceinline__ unsigned xb_ld(unsigned* p)              { return __hip_atomic_load(p, __ATOMIC_RELAXED, __HIP_MEMORY_SCOPE_AGENT); }
; __device__ __forceinline__ unsigned xb_add(unsigned* p, unsigned v) { return __hip_atomic_fetch_add(p, v, __ATOMIC_RELAXED, __HIP_MEMORY_SCOPE_AGENT); }
; #define XB_SPIN(cond, bar) do { unsigned _sp = 0; while (cond) { __builtin_amdgcn_s_sleep(1); \
;     if ((++_sp & 255u) == 0u) { if (xb_ld(&(bar)[XB_TMO])) break; if (_sp > XB_SPIN_CAP) { atomicAdd(&(bar)[XB_TMO], 1u); break; } } } } while (0)
; __device__ __forceinline__ void xcd_barrier(const XcdBarrier& b) {
;   asm volatile("s_waitcnt vmcnt(0)" ::: "memory");
;   __syncthreads();
;   if (threadIdx.x == 0) {
;     unsigned* bar = b.bar;
;     __builtin_amdgcn_s_waitcnt(0);
;     unsigned nloc = b.st[0], nx = b.st[1];
;     if (nloc == 0u) { xcd_barrier_complete(bar, b.x, nloc, nx); b.st[0] = nloc; b.st[1] = nx; }
;     const unsigned old = xb_add(&bar[XB_XSUB(b.x)], 1u);
;     const unsigned gen = old / nloc;
;     if (old + 1u == (gen + 1u) * nloc) {
;       __builtin_amdgcn_fence(__ATOMIC_RELEASE, "agent");
;       asm volatile("s_waitcnt vmcnt(0)" ::: "memory");
;       const unsigned og = xb_add(&bar[XB_TOP], 1u);
;       const unsigned tg = og / nx;
;       if (og + 1u == (tg + 1u) * nx) xb_add(&bar[XB_TOPGEN], 1u);
;       else XB_SPIN(xb_ld(&bar[XB_TOPGEN]) == tg, bar);
;       __builtin_amdgcn_fence(__ATOMIC_ACQUIRE, "agent");
;       xb_add(&bar[XB_XGEN(b.x)], 1u);
;       asm volatile("s_waitcnt vmcnt(0)" ::: "memory");
;     } else {
;       XB_SPIN(xb_ld(&bar[XB_XGEN(b.x)]) == gen, bar);
;       __builtin_amdgcn_fence(__ATOMIC_ACQUIRE, "agent");
;       asm volatile("s_waitcnt vmcnt(0)" ::: "memory");
;     }
;   }
;   __syncthreads();
; }
.LBB0_1131:
	s_or_b64 exec, exec, s[20:21]
	s_waitcnt vmcnt(0)
	s_barrier
	s_and_saveexec_b64 s[8:9], s[4:5]
	s_cbranch_execz .LBB0_1183
	s_waitcnt vmcnt(0) lgkmcnt(0)
	s_add_u32 s98, s98, 1
	v_mov_b32_e32 v253, 0x12810
	ds_read_b32 v254, v253
	ds_read_b32 v253, v253 offset:4
	s_lshl_b32 s101, s33, 8
	s_add_u32 s99, s101, 5120
	s_waitcnt lgkmcnt(0)
	v_readfirstlane_b32 s100, v254
	v_mov_b32_e32 v254, s99
	v_readfirstlane_b32 s99, v253
	s_nop 0
	v_mov_b32_e32 v253, v254
	v_mov_b32_e32 v254, 1
	buffer_inv sc1
	global_atomic_add v254, v253, v254, s[44:45] offset:64 sc0
	s_mul_i32 s100, s100, s98
	s_mul_i32 s99, s99, s98
	s_waitcnt vmcnt(0)
	v_add_u32_e32 v254, 1, v254
	v_cmp_ne_u32_e32 vcc, s100, v254
	s_cbranch_vccnz .Lgb_wait_9
	buffer_wbl2 sc1
	s_waitcnt vmcnt(0)
	v_mov_b32_e32 v254, 1
	v_mov_b32_e32 v253, 9216
	global_atomic_add v253, v254, s[44:45] offset:64
	global_atomic_add v253, v254, s[44:45] offset:320
	global_atomic_add v253, v254, s[44:45] offset:576
	global_atomic_add v253, v254, s[44:45] offset:832
	global_atomic_add v253, v254, s[44:45] offset:1088
	global_atomic_add v253, v254, s[44:45] offset:1344
	global_atomic_add v253, v254, s[44:45] offset:1600
	global_atomic_add v253, v254, s[44:45] offset:1856
	v_mov_b32_e32 v253, 11264
	global_atomic_add v253, v254, s[44:45] offset:64
	global_atomic_add v253, v254, s[44:45] offset:320
	global_atomic_add v253, v254, s[44:45] offset:576
	global_atomic_add v253, v254, s[44:45] offset:832
	global_atomic_add v253, v254, s[44:45] offset:1088
	global_atomic_add v253, v254, s[44:45] offset:1344
	global_atomic_add v253, v254, s[44:45] offset:1600
	global_atomic_add v253, v254, s[44:45] offset:1856

; __device__ __forceinline__ unsigned xb_ld(unsigned* p)              { return __hip_atomic_load(p, __ATOMIC_RELAXED, __HIP_MEMORY_SCOPE_AGENT); }
; __device__ __forceinline__ unsigned xb_add(unsigned* p, unsigned v) { return __hip_atomic_fetch_add(p, v, __ATOMIC_RELAXED, __HIP_MEMORY_SCOPE_AGENT); }
; #define XB_SPIN(cond, bar) do { unsigned _sp = 0; while (cond) { __builtin_amdgcn_s_sleep(1); \
;     if ((++_sp & 255u) == 0u) { if (xb_ld(&(bar)[XB_TMO])) break; if (_sp > XB_SPIN_CAP) { atomicAdd(&(bar)[XB_TMO], 1u); break; } } } } while (0)
; __device__ __forceinline__ void xcd_barrier(const XcdBarrier& b) {
;   asm volatile("s_waitcnt vmcnt(0)" ::: "memory");
;   __syncthreads();
;   if (threadIdx.x == 0) {
;     unsigned* bar = b.bar;
;     __builtin_amdgcn_s_waitcnt(0);
;     unsigned nloc = b.st[0], nx = b.st[1];
;     if (nloc == 0u) { xcd_barrier_complete(bar, b.x, nloc, nx); b.st[0] = nloc; b.st[1] = nx; }
;     const unsigned old = xb_add(&bar[XB_XSUB(b.x)], 1u);
;     const unsigned gen = old / nloc;
;     if (old + 1u == (gen + 1u) * nloc) {
;       __builtin_amdgcn_fence(__ATOMIC_RELEASE, "agent");
;       asm volatile("s_waitcnt vmcnt(0)" ::: "memory");
;       const unsigned og = xb_add(&bar[XB_TOP], 1u);
;       const unsigned tg = og / nx;
;       if (og + 1u == (tg + 1u) * nx) xb_add(&bar[XB_TOPGEN], 1u);
;       else XB_SPIN(xb_ld(&bar[XB_TOPGEN]) == tg, bar);
;       __builtin_amdgcn_fence(__ATOMIC_ACQUIRE, "agent");
;       xb_add(&bar[XB_XGEN(b.x)], 1u);
;       asm volatile("s_waitcnt vmcnt(0)" ::: "memory");
;     } else {
;       XB_SPIN(xb_ld(&bar[XB_XGEN(b.x)]) == gen, bar);
;       __builtin_amdgcn_fence(__ATOMIC_ACQUIRE, "agent");
;       asm volatile("s_waitcnt vmcnt(0)" ::: "memory");
;     }
;   }
;   __syncthreads();
; }
.LBB0_1196:
	s_waitcnt vmcnt(0)
	s_barrier
	s_and_saveexec_b64 s[2:3], s[4:5]
	s_cbranch_execz .LBB0_1248
	s_waitcnt vmcnt(0) lgkmcnt(0)
	s_add_u32 s98, s98, 1
	v_mov_b32_e32 v253, 0x12810
	ds_read_b32 v254, v253
	ds_read_b32 v253, v253 offset:4
	s_lshl_b32 s101, s33, 8
	s_add_u32 s99, s101, 5120
	s_waitcnt lgkmcnt(0)
	v_readfirstlane_b32 s100, v254
	v_mov_b32_e32 v254, s99
	v_readfirstlane_b32 s99, v253
	s_nop 0
	v_mov_b32_e32 v253, v254
	v_mov_b32_e32 v254, 1
	buffer_inv sc1
	global_atomic_add v254, v253, v254, s[44:45] offset:64 sc0
	s_mul_i32 s100, s100, s98
	s_mul_i32 s99, s99, s98
	s_waitcnt vmcnt(0)
	v_add_u32_e32 v254, 1, v254
	v_cmp_ne_u32_e32 vcc, s100, v254
	s_cbranch_vccnz .Lgb_wait_10
	buffer_wbl2 sc1
	s_waitcnt vmcnt(0)
	v_mov_b32_e32 v254, 1
	v_mov_b32_e32 v253, 9216
	global_atomic_add v253, v254, s[44:45] offset:64
	global_atomic_add v253, v254, s[44:45] offset:320
	global_atomic_add v253, v254, s[44:45] offset:576
	global_atomic_add v253, v254, s[44:45] offset:832
	global_atomic_add v253, v254, s[44:45] offset:1088
	global_atomic_add v253, v254, s[44:45] offset:1344
	global_atomic_add v253, v254, s[44:45] offset:1600
	global_atomic_add v253, v254, s[44:45] offset:1856
	v_mov_b32_e32 v253, 11264
	global_atomic_add v253, v254, s[44:45] offset:64
	global_atomic_add v253, v254, s[44:45] offset:320
	global_atomic_add v253, v254, s[44:45] offset:576
	global_atomic_add v253, v254, s[44:45] offset:832
	global_atomic_add v253, v254, s[44:45] offset:1088
	global_atomic_add v253, v254, s[44:45] offset:1344
	global_atomic_add v253, v254, s[44:45] offset:1600
	global_atomic_add v253, v254, s[44:45] offset:1856

; __device__ __forceinline__ unsigned xb_ld(unsigned* p)              { return __hip_atomic_load(p, __ATOMIC_RELAXED, __HIP_MEMORY_SCOPE_AGENT); }
; __device__ __forceinline__ unsigned xb_add(unsigned* p, unsigned v) { return __hip_atomic_fetch_add(p, v, __ATOMIC_RELAXED, __HIP_MEMORY_SCOPE_AGENT); }
; #define XB_SPIN(cond, bar) do { unsigned _sp = 0; while (cond) { __builtin_amdgcn_s_sleep(1); \
;     if ((++_sp & 255u) == 0u) { if (xb_ld(&(bar)[XB_TMO])) break; if (_sp > XB_SPIN_CAP) { atomicAdd(&(bar)[XB_TMO], 1u); break; } } } } while (0)
; __device__ __forceinline__ void xcd_barrier(const XcdBarrier& b) {
;   asm volatile("s_waitcnt vmcnt(0)" ::: "memory");
;   __syncthreads();
;   if (threadIdx.x == 0) {
;     unsigned* bar = b.bar;
;     __builtin_amdgcn_s_waitcnt(0);
;     unsigned nloc = b.st[0], nx = b.st[1];
;     if (nloc == 0u) { xcd_barrier_complete(bar, b.x, nloc, nx); b.st[0] = nloc; b.st[1] = nx; }
;     const unsigned old = xb_add(&bar[XB_XSUB(b.x)], 1u);
;     const unsigned gen = old / nloc;
;     if (old + 1u == (gen + 1u) * nloc) {
;       __builtin_amdgcn_fence(__ATOMIC_RELEASE, "agent");
;       asm volatile("s_waitcnt vmcnt(0)" ::: "memory");
;       const unsigned og = xb_add(&bar[XB_TOP], 1u);
;       const unsigned tg = og / nx;
;       if (og + 1u == (tg + 1u) * nx) xb_add(&bar[XB_TOPGEN], 1u);
;       else XB_SPIN(xb_ld(&bar[XB_TOPGEN]) == tg, bar);
;       __builtin_amdgcn_fence(__ATOMIC_ACQUIRE, "agent");
;       xb_add(&bar[XB_XGEN(b.x)], 1u);
;       asm volatile("s_waitcnt vmcnt(0)" ::: "memory");
;     } else {
;       XB_SPIN(xb_ld(&bar[XB_XGEN(b.x)]) == gen, bar);
;       __builtin_amdgcn_fence(__ATOMIC_ACQUIRE, "agent");
;       asm volatile("s_waitcnt vmcnt(0)" ::: "memory");
;     }
;   }
;   __syncthreads();
; }
.LBB0_1327:
	s_or_b64 exec, exec, s[2:3]
	s_waitcnt vmcnt(0)
	s_barrier
	s_and_saveexec_b64 s[2:3], s[4:5]
	s_cbranch_execz .LBB0_1379
	s_waitcnt vmcnt(0) lgkmcnt(0)
	s_add_u32 s98, s98, 1
	v_mov_b32_e32 v253, 0x12810
	ds_read_b32 v254, v253
	ds_read_b32 v253, v253 offset:4
	s_lshl_b32 s101, s33, 8
	s_add_u32 s99, s101, 5120
	s_waitcnt lgkmcnt(0)
	v_readfirstlane_b32 s100, v254
	v_mov_b32_e32 v254, s99
	v_readfirstlane_b32 s99, v253
	s_nop 0
	v_mov_b32_e32 v253, v254
	v_mov_b32_e32 v254, 1
	buffer_inv sc1
	global_atomic_add v254, v253, v254, s[44:45] offset:64 sc0
	s_mul_i32 s100, s100, s98
	s_mul_i32 s99, s99, s98
	s_waitcnt vmcnt(0)
	v_add_u32_e32 v254, 1, v254
	v_cmp_ne_u32_e32 vcc, s100, v254
	s_cbranch_vccnz .Lgb_wait_12
	buffer_wbl2 sc1
	s_waitcnt vmcnt(0)
	v_mov_b32_e32 v254, 1
	v_mov_b32_e32 v253, 9216
	global_atomic_add v253, v254, s[44:45] offset:64
	global_atomic_add v253, v254, s[44:45] offset:320
	global_atomic_add v253, v254, s[44:45] offset:576
	global_atomic_add v253, v254, s[44:45] offset:832
	global_atomic_add v253, v254, s[44:45] offset:1088
	global_atomic_add v253, v254, s[44:45] offset:1344
	global_atomic_add v253, v254, s[44:45] offset:1600
	global_atomic_add v253, v254, s[44:45] offset:1856
	v_mov_b32_e32 v253, 11264
	global_atomic_add v253, v254, s[44:45] offset:64
	global_atomic_add v253, v254, s[44:45] offset:320
	global_atomic_add v253, v254, s[44:45] offset:576
	global_atomic_add v253, v254, s[44:45] offset:832
	global_atomic_add v253, v254, s[44:45] offset:1088
	global_atomic_add v253, v254, s[44:45] offset:1344
	global_atomic_add v253, v254, s[44:45] offset:1600
	global_atomic_add v253, v254, s[44:45] offset:1856
